# ret-scan: software-pipelined LDS fragment reads in step 1a/1b/2b (was read-wait-mfma serialized)
# speedup vs baseline: 1.0034x; 1.0034x over previous
; #define RS_MMA2(fa, fb) do { _Pragma("unroll") for (int j = 0; j < 2; ++j) acc = mfma32(fa[j], fb[j], acc); } while (0)
; #define RS_LD1B(fa, fb, g4) do { _Pragma("unroll") for (int j = 0; j < 2; ++j) { const int ks = 2 * (g4) + j; \
;                     fa[j] = *(const LAS s16x8*)(lds + QN + (32 * ti + a31) * QRS + (16 * ks + 8 * a5) * 2); \
;                     fb[j] = *(const LAS s16x8*)(lds + ST + (32 * vi + a31) * SRS + (16 * ks + 8 * a5) * 2); } } while (0)
; __device__ __forceinline__ void phase_ret_scan(const bf16* PROJ, bf16* O, LAS unsigned char* lds, int tid, int vcu, int G) {
;     ...
;             } else {
;                 const int ti = t_i, vi = x_i;
;     ...
;                 RS_LD1B(fa0, fb0, 0); RS_LD1B(fa1, fb1, 1);
; #pragma unroll
;                 for (int g2 = 0; g2 < 3; ++g2) { RS_MMA2(fa0, fb0); RS_LD1B(fa0, fb0, 2 * g2 + 2); RS_MMA2(fa1, fb1); RS_LD1B(fa1, fb1, 2 * g2 + 3); }
;                 RS_MMA2(fa0, fb0); RS_MMA2(fa1, fb1);
;     ...
; #pragma unroll
;                 for (int r = 0; r < 16; ++r) acc[r] *= dec[r];
.LBB0_643:
	v_mov_b32_e32 v2, v166
	s_and_b64 vcc, exec, s[74:75]
	v_and_b32_e32 v0, 31, v2
	v_ashrrev_i32_e32 v3, 5, v2
	s_mov_b64 s[4:5], -1
	s_cbranch_vccnz .LBB0_645
	v_or_b32_e32 v4, s12, v0
	v_mul_u32_u24_e32 v4, 0x210, v4
	v_lshlrev_b32_e32 v8, 4, v3
	v_add3_u32 v12, 0, v4, v8
	v_or_b32_e32 v9, s13, v0
	v_mul_u32_u24_e32 v9, 0x210, v9
	s_add_i32 s4, 0, 0x16800
	v_add3_u32 v13, s4, v9, v8
	s_mov_b64 s[4:5], 0
	ds_read_b128 v[16:19], v12
	ds_read_b128 v[20:23], v13
	ds_read_b128 v[24:27], v12 offset:32
	ds_read_b128 v[28:31], v13 offset:32
	ds_read_b128 v[32:35], v12 offset:64
	ds_read_b128 v[36:39], v13 offset:64
	ds_read_b128 v[40:43], v12 offset:96
	ds_read_b128 v[44:47], v13 offset:96
	ds_read_b128 v[48:51], v12 offset:128
	ds_read_b128 v[52:55], v13 offset:128
	ds_read_b128 v[56:59], v12 offset:160
	ds_read_b128 v[60:63], v13 offset:160
	s_waitcnt lgkmcnt(10)
	v_mfma_f32_32x32x16_bf16 v[80:95], v[16:19], v[20:23], 0
	ds_read_b128 v[16:19], v12 offset:192
	ds_read_b128 v[20:23], v13 offset:192
	s_waitcnt lgkmcnt(10)
	v_mfma_f32_32x32x16_bf16 v[80:95], v[24:27], v[28:31], v[80:95]
	ds_read_b128 v[24:27], v12 offset:224
	ds_read_b128 v[28:31], v13 offset:224
	s_waitcnt lgkmcnt(10)
	v_mfma_f32_32x32x16_bf16 v[80:95], v[32:35], v[36:39], v[80:95]
	ds_read_b128 v[32:35], v12 offset:256
	ds_read_b128 v[36:39], v13 offset:256
	s_waitcnt lgkmcnt(10)
	v_mfma_f32_32x32x16_bf16 v[80:95], v[40:43], v[44:47], v[80:95]
	ds_read_b128 v[40:43], v12 offset:288
	ds_read_b128 v[44:47], v13 offset:288
	s_waitcnt lgkmcnt(10)
	v_mfma_f32_32x32x16_bf16 v[80:95], v[48:51], v[52:55], v[80:95]
	ds_read_b128 v[48:51], v12 offset:320
	ds_read_b128 v[52:55], v13 offset:320
	s_waitcnt lgkmcnt(10)
	v_mfma_f32_32x32x16_bf16 v[80:95], v[56:59], v[60:63], v[80:95]
	ds_read_b128 v[56:59], v12 offset:352
	ds_read_b128 v[60:63], v13 offset:352
	s_waitcnt lgkmcnt(10)
	v_mfma_f32_32x32x16_bf16 v[80:95], v[16:19], v[20:23], v[80:95]
	ds_read_b128 v[16:19], v12 offset:384
	ds_read_b128 v[20:23], v13 offset:384
	s_waitcnt lgkmcnt(10)
	v_mfma_f32_32x32x16_bf16 v[80:95], v[24:27], v[28:31], v[80:95]
	ds_read_b128 v[24:27], v12 offset:416
	ds_read_b128 v[28:31], v13 offset:416
	s_waitcnt lgkmcnt(10)
	v_mfma_f32_32x32x16_bf16 v[80:95], v[32:35], v[36:39], v[80:95]
	ds_read_b128 v[32:35], v12 offset:448
	ds_read_b128 v[36:39], v13 offset:448
	s_waitcnt lgkmcnt(10)
	v_mfma_f32_32x32x16_bf16 v[80:95], v[40:43], v[44:47], v[80:95]
	ds_read_b128 v[40:43], v12 offset:480
	ds_read_b128 v[44:47], v13 offset:480
	s_waitcnt lgkmcnt(10)
	v_mfma_f32_32x32x16_bf16 v[80:95], v[48:51], v[52:55], v[80:95]
	s_waitcnt lgkmcnt(8)
	v_mfma_f32_32x32x16_bf16 v[80:95], v[56:59], v[60:63], v[80:95]
	s_waitcnt lgkmcnt(6)
	v_mfma_f32_32x32x16_bf16 v[80:95], v[16:19], v[20:23], v[80:95]
	s_waitcnt lgkmcnt(4)
	v_mfma_f32_32x32x16_bf16 v[80:95], v[24:27], v[28:31], v[80:95]
	s_waitcnt lgkmcnt(2)
	v_mfma_f32_32x32x16_bf16 v[80:95], v[32:35], v[36:39], v[80:95]
	s_waitcnt lgkmcnt(0)
	v_mfma_f32_32x32x16_bf16 v[80:95], v[40:43], v[44:47], v[80:95]
	s_nop 11
	v_pk_mul_f32 v[94:95], v[146:147], v[94:95]
	v_pk_mul_f32 v[92:93], v[144:145], v[92:93]
	v_pk_mul_f32 v[90:91], v[142:143], v[90:91]
	v_pk_mul_f32 v[88:89], v[140:141], v[88:89]
	v_pk_mul_f32 v[86:87], v[138:139], v[86:87]
	v_pk_mul_f32 v[84:85], v[136:137], v[84:85]
	v_pk_mul_f32 v[82:83], v[134:135], v[82:83]
	v_pk_mul_f32 v[80:81], v[132:133], v[80:81]
; #define LAS __attribute__((address_space(3)))
; __device__ __forceinline__ unsigned pk2(float lo, float hi) { const pk_f2 v = {lo, hi}; return __builtin_bit_cast(unsigned, __builtin_convertvector(v, pk_b2)); }
; #define RS_LD1A(fa, fb, g4) do { _Pragma("unroll") for (int j = 0; j < 2; ++j) { const int ks = 2 * (g4) + j; \
;                     fa[j] = *(const LAS s16x8*)(lds + KN + (ks >> 3) * 16384 + off_b(32 * si + a31, 2 * (ks & 7) + a5)); \
;                     fb[j] = *(const LAS s16x8*)(lds + QN + (32 * ti + a31) * QRS + (16 * ks + 8 * a5) * 2); } } while (0)
; #define RS_MMA4(fa, fb) do { _Pragma("unroll") for (int j = 0; j < 4; ++j) acc = mfma32(fa[j], fb[j], acc); } while (0)
; #define RS_MMA2(fa, fb) do { _Pragma("unroll") for (int j = 0; j < 2; ++j) acc = mfma32(fa[j], fb[j], acc); } while (0)
; __device__ __forceinline__ void phase_ret_scan(const bf16* PROJ, bf16* O, LAS unsigned char* lds, int tid, int vcu, int G) {
;     ...
;             if (wave < 4) {
;                 const int si = t_i, ti = x_i;
;     ...
;                 RS_LD1A(fa0, fb0, 0); RS_LD1A(fa1, fb1, 1);
; #pragma unroll
;                 for (int g2 = 0; g2 < 3; ++g2) { RS_MMA2(fa0, fb0); RS_LD1A(fa0, fb0, 2 * g2 + 2); RS_MMA2(fa1, fb1); RS_LD1A(fa1, fb1, 2 * g2 + 3); }
;                 RS_MMA2(fa0, fb0); RS_MMA2(fa1, fb1);
;     ...
;                 const int t = 32 * ti + a31;
; #pragma unroll
;                 for (int g = 0; g < 4; ++g) { float pvv[4];
; #pragma unroll
;                     for (int e = 0; e < 4; ++e) pvv[e] = acc[4 * g + e] * dec[4 * g + e];
;                     v2u w; w.x = pk2(pvv[0], pvv[1]); w.y = pk2(pvv[2], pvv[3]);
;                     *(LAS v2u*)(lds + PI + t * PRS + (32 * si + 8 * g + 4 * a5) * 2) = w; }
;     ...
;             } else {
;                 const int ti = t_i, vi = x_i;
; #pragma unroll
;                 for (int ks = 0; ks < 4; ++ks) { fa0[ks] = *(const LAS s16x8*)(lds + PI + (32 * ti + a31) * PRS + (16 * ks + 8 * a5) * 2); fb0[ks] = tr_frag_b2(lds + VV, trb_base(lnA, vi, 0), trb_base(lnA, vi, 1), ks); }
;                 RS_MMA4(fa0, fb0);
; #pragma unroll
;                 for (int i = 0; i < 8; ++i) { const float o0_ = acc[2 * i], o1_ = acc[2 * i + 1]; opk[i] = pk2(o0_, o1_); }
;             }
.LBB0_645:
	s_andn2_b64 vcc, exec, s[4:5]
	s_cbranch_vccnz .LBB0_647
	v_lshlrev_b32_e32 v4, 2, v0
	v_and_b32_e32 v12, 12, v4
	v_bfe_u32 v13, v2, 2, 2
	v_lshl_add_u32 v14, v0, 8, s14
	v_bitop3_b32 v4, v12, v3, v13 bitop3:0x36
	v_readlane_b32 s4, v250, 13
	v_lshl_add_u32 v243, v4, 4, v14
	v_or_b32_e32 v15, s13, v0
	v_mul_u32_u24_e32 v8, 0x210, v15
	v_lshlrev_b32_e32 v9, 4, v3
	v_add3_u32 v242, 0, v8, v9
	v_lshlrev_b32_e32 v246, 3, v3
	v_mov_b32_e32 v247, s4
	s_movk_i32 s4, 0x90
	v_mad_u32_u24 v247, v15, s4, v247
	v_add3_u32 v149, v247, v246, s15
	ds_read_b128 v[4:7], v243 offset:33792
	ds_read_b128 v[8:11], v242
	v_xor_b32_e32 v245, 32, v243
	ds_read_b128 v[12:15], v245 offset:33792
	ds_read_b128 v[226:229], v242 offset:32
	v_xor_b32_e32 v244, 64, v243
	ds_read_b128 v[230:233], v244 offset:33792
	ds_read_b128 v[238:241], v242 offset:64
	s_waitcnt lgkmcnt(4)
	v_mfma_f32_32x32x16_bf16 v[80:95], v[4:7], v[8:11], 0
	v_xor_b32_e32 v245, 0x60, v243
	ds_read_b128 v[4:7], v245 offset:33792
	ds_read_b128 v[8:11], v242 offset:96
	s_waitcnt lgkmcnt(4)
	v_mfma_f32_32x32x16_bf16 v[80:95], v[12:15], v[226:229], v[80:95]
	v_xor_b32_e32 v244, 0x80, v243
	ds_read_b128 v[12:15], v244 offset:33792
	ds_read_b128 v[226:229], v242 offset:128
	s_waitcnt lgkmcnt(4)
	v_mfma_f32_32x32x16_bf16 v[80:95], v[230:233], v[238:241], v[80:95]
	v_xor_b32_e32 v245, 0xa0, v243
	ds_read_b128 v[230:233], v245 offset:33792
	ds_read_b128 v[238:241], v242 offset:160
	s_waitcnt lgkmcnt(4)
	v_mfma_f32_32x32x16_bf16 v[80:95], v[4:7], v[8:11], v[80:95]
	v_xor_b32_e32 v244, 0xc0, v243
	ds_read_b128 v[4:7], v244 offset:33792
	ds_read_b128 v[8:11], v242 offset:192
	s_waitcnt lgkmcnt(4)
	v_mfma_f32_32x32x16_bf16 v[80:95], v[12:15], v[226:229], v[80:95]
	v_xor_b32_e32 v245, 0xe0, v243
	ds_read_b128 v[12:15], v245 offset:33792
	ds_read_b128 v[226:229], v242 offset:224
	s_waitcnt lgkmcnt(4)
	v_mfma_f32_32x32x16_bf16 v[80:95], v[230:233], v[238:241], v[80:95]
	ds_read_b128 v[230:233], v243 offset:50176
	ds_read_b128 v[238:241], v242 offset:256
	s_waitcnt lgkmcnt(4)
	v_mfma_f32_32x32x16_bf16 v[80:95], v[4:7], v[8:11], v[80:95]
	v_xor_b32_e32 v245, 32, v243
	ds_read_b128 v[4:7], v245 offset:50176
	ds_read_b128 v[8:11], v242 offset:288
	s_waitcnt lgkmcnt(4)
	v_mfma_f32_32x32x16_bf16 v[80:95], v[12:15], v[226:229], v[80:95]
	v_xor_b32_e32 v244, 64, v243
	ds_read_b128 v[12:15], v244 offset:50176
	ds_read_b128 v[226:229], v242 offset:320
	s_waitcnt lgkmcnt(4)
	v_mfma_f32_32x32x16_bf16 v[80:95], v[230:233], v[238:241], v[80:95]
	v_xor_b32_e32 v245, 0x60, v243
	ds_read_b128 v[230:233], v245 offset:50176
	ds_read_b128 v[238:241], v242 offset:352
	s_waitcnt lgkmcnt(4)
	v_mfma_f32_32x32x16_bf16 v[80:95], v[4:7], v[8:11], v[80:95]
	v_xor_b32_e32 v244, 0x80, v243
	ds_read_b128 v[4:7], v244 offset:50176
	ds_read_b128 v[8:11], v242 offset:384
	s_waitcnt lgkmcnt(4)
	v_mfma_f32_32x32x16_bf16 v[80:95], v[12:15], v[226:229], v[80:95]
	v_xor_b32_e32 v245, 0xa0, v243
	ds_read_b128 v[12:15], v245 offset:50176
	ds_read_b128 v[226:229], v242 offset:416
	s_waitcnt lgkmcnt(4)
	v_mfma_f32_32x32x16_bf16 v[80:95], v[230:233], v[238:241], v[80:95]
	v_xor_b32_e32 v244, 0xc0, v243
	ds_read_b128 v[230:233], v244 offset:50176
	ds_read_b128 v[238:241], v242 offset:448
	s_waitcnt lgkmcnt(4)
	v_mfma_f32_32x32x16_bf16 v[80:95], v[4:7], v[8:11], v[80:95]
	v_xor_b32_e32 v245, 0xe0, v243
	ds_read_b128 v[4:7], v245 offset:50176
	ds_read_b128 v[8:11], v242 offset:480
	s_waitcnt lgkmcnt(4)
	v_mfma_f32_32x32x16_bf16 v[80:95], v[12:15], v[226:229], v[80:95]
	s_waitcnt lgkmcnt(2)
	v_mfma_f32_32x32x16_bf16 v[80:95], v[230:233], v[238:241], v[80:95]
	s_waitcnt lgkmcnt(0)
	v_mfma_f32_32x32x16_bf16 v[80:95], v[4:7], v[8:11], v[80:95]
	s_nop 11
	v_pk_mul_f32 v[4:5], v[132:133], v[80:81]
	v_pk_mul_f32 v[6:7], v[134:135], v[82:83]
	v_pk_mul_f32 v[8:9], v[136:137], v[84:85]
	v_pk_mul_f32 v[10:11], v[138:139], v[86:87]
	v_pk_mul_f32 v[12:13], v[140:141], v[88:89]
	v_pk_mul_f32 v[14:15], v[142:143], v[90:91]
	v_pk_mul_f32 v[238:239], v[144:145], v[92:93]
	v_pk_mul_f32 v[240:241], v[146:147], v[94:95]
	v_cvt_pk_bf16_f32 v4, v4, v5
	v_cvt_pk_bf16_f32 v5, v6, v7
	v_cvt_pk_bf16_f32 v6, v8, v9
	v_cvt_pk_bf16_f32 v7, v10, v11
	v_cvt_pk_bf16_f32 v8, v12, v13
	v_cvt_pk_bf16_f32 v9, v14, v15
	v_cvt_pk_bf16_f32 v10, v238, v239
	v_cvt_pk_bf16_f32 v11, v240, v241
	ds_write2_b64 v149, v[4:5], v[6:7] offset1:2
	ds_write2_b64 v149, v[8:9], v[10:11] offset0:4 offset1:6
.LBB0_647:
	s_and_b64 vcc, exec, s[74:75]
	s_mov_b64 s[8:9], -1
	s_waitcnt lgkmcnt(0)
	s_barrier
	s_cbranch_vccnz .LBB0_649
	v_or_b32_e32 v4, s12, v0
	v_mul_u32_u24_e32 v4, 0x90, v4
	v_lshlrev_b32_e32 v5, 4, v3
	v_readlane_b32 s4, v250, 13
	v_bfe_u32 v6, v2, 1, 1
	s_mov_b64 s[8:9], 0
	v_add3_u32 v12, s4, v4, v5
	v_bfe_u32 v4, v2, 2, 2
	v_lshlrev_b32_e32 v5, 11, v3
	v_lshl_or_b32 v8, v4, 8, v5
	v_lshrrev_b32_e32 v5, 3, v2
	v_and_b32_e32 v5, 2, v5
	v_or3_b32 v5, v5, s16, v6
	v_lshlrev_b32_e32 v6, 1, v3
	v_lshlrev_b32_e32 v4, 2, v4
	v_and_b32_e32 v6, 2, v6
	v_or_b32_e32 v7, v6, v4
	v_bitop3_b32 v4, v6, v5, v4 bitop3:0x36
	v_lshlrev_b32_e32 v6, 3, v2
	v_readlane_b32 s4, v250, 12
	v_and_b32_e32 v9, 8, v6
	v_bitop3_b32 v10, v7, v5, 1 bitop3:0x36
	v_lshl_add_u32 v4, v4, 4, s4
	v_add3_u32 v13, v4, v8, v9
	v_lshl_add_u32 v10, v10, 4, s4
	v_add3_u32 v14, v10, v8, v9
	ds_read_b128 v[16:19], v12
	ds_read_b64_tr_b16 v[32:33], v13
	ds_read_b64_tr_b16 v[34:35], v14 offset:1024
	ds_read_b128 v[20:23], v12 offset:32
	ds_read_b64_tr_b16 v[36:37], v13 offset:4096
	ds_read_b64_tr_b16 v[38:39], v14 offset:5120
	ds_read_b128 v[24:27], v12 offset:64
	ds_read_b64_tr_b16 v[40:41], v13 offset:8192
	ds_read_b64_tr_b16 v[42:43], v14 offset:9216
	ds_read_b128 v[28:31], v12 offset:96
	ds_read_b64_tr_b16 v[44:45], v13 offset:12288
	ds_read_b64_tr_b16 v[46:47], v14 offset:13312
	s_waitcnt lgkmcnt(9)
	v_mfma_f32_32x32x16_bf16 v[80:95], v[16:19], v[32:35], v[80:95]
	s_waitcnt lgkmcnt(6)
	v_mfma_f32_32x32x16_bf16 v[80:95], v[20:23], v[36:39], v[80:95]
	s_waitcnt lgkmcnt(3)
	v_mfma_f32_32x32x16_bf16 v[80:95], v[24:27], v[40:43], v[80:95]
	s_waitcnt lgkmcnt(0)
	v_mfma_f32_32x32x16_bf16 v[80:95], v[28:31], v[44:47], v[80:95]
	s_nop 11
	v_cvt_pk_bf16_f32 v4, v80, v81
	v_cvt_pk_bf16_f32 v5, v82, v83
	v_cvt_pk_bf16_f32 v6, v84, v85
	v_cvt_pk_bf16_f32 v7, v86, v87
	v_cvt_pk_bf16_f32 v8, v88, v89
	v_cvt_pk_bf16_f32 v9, v90, v91
	v_cvt_pk_bf16_f32 v10, v92, v93
	v_cvt_pk_bf16_f32 v11, v94, v95
